# baseline (speedup 1.0000x reference)
.Lc1_back0:
	v_pk_fma_f16 v6, v2, v138, v139 op_sel:[0,1,1] op_sel_hi:[1,1,1] neg_lo:[1,0,0] neg_hi:[1,0,0]
	v_pk_fma_f16 v7, v3, v138, v139 op_sel:[0,1,1] op_sel_hi:[1,1,1] neg_lo:[1,0,0] neg_hi:[1,0,0]
	v_pk_fma_f16 v8, v4, v138, v139 op_sel:[0,1,1] op_sel_hi:[1,1,1] neg_lo:[1,0,0] neg_hi:[1,0,0]
	v_pk_fma_f16 v9, v5, v138, v139 op_sel:[0,1,1] op_sel_hi:[1,1,1] neg_lo:[1,0,0] neg_hi:[1,0,0]
	v_mfma_f32_16x16x32_f16 v[22:25], v[10:13], v[2:5], 0
	ds_read2_b64 v[108:111], v32 offset0:15 offset1:217
	v_pk_fma_f16 v2, v84, v6, v2
	v_pk_fma_f16 v3, v85, v7, v3
	v_pk_fma_f16 v4, v86, v8, v4
	v_pk_fma_f16 v5, v87, v9, v5
	v_cndmask_b32_e64 v26, v26, v18, s[64:65]
	s_waitcnt lgkmcnt(6)
	v_pk_fma_f16 v6, v2, v140, v141 op_sel:[0,1,1] op_sel_hi:[1,1,1] neg_lo:[1,0,0] neg_hi:[1,0,0]
	v_pk_fma_f16 v7, v3, v140, v141 op_sel:[0,1,1] op_sel_hi:[1,1,1] neg_lo:[1,0,0] neg_hi:[1,0,0]
	v_pk_fma_f16 v8, v4, v140, v141 op_sel:[0,1,1] op_sel_hi:[1,1,1] neg_lo:[1,0,0] neg_hi:[1,0,0]
	v_pk_fma_f16 v9, v5, v140, v141 op_sel:[0,1,1] op_sel_hi:[1,1,1] neg_lo:[1,0,0] neg_hi:[1,0,0]
	v_mfma_f32_16x16x32_f16 v[18:21], v[10:13], v[2:5], 0
	ds_read2_b64 v[48:51], v32 offset0:16 offset1:218
	ds_read_b128 v[120:123], v33 offset:128
	ds_read2_b64 v[14:17], v34 offset0:16 offset1:218
	v_pk_fma_f16 v2, v88, v6, v2
	v_pk_fma_f16 v3, v89, v7, v3
	v_pk_fma_f16 v4, v90, v8, v4
	v_pk_fma_f16 v5, v91, v9, v5
	v_cndmask_b32_e64 v27, v27, v23, s[64:65]
	s_mov_b32 s72, 0
	s_cmp_eq_u32 s70, 0
	s_cbranch_scc1 .Lc1_nd0
	s_cmp_eq_u32 s36, 3
	s_cbranch_scc0 .Lc1_nd0
	s_mov_b32 s72, 1
	ds_read_b32 v45, v36 offset:124
	ds_read_b128 v[112:115], v43 offset:0
	ds_read_b128 v[116:119], v43 offset:1024
.Lc1_nd0:
	v_pk_fma_f16 v6, v2, v142, v143 op_sel:[0,1,1] op_sel_hi:[1,1,1] neg_lo:[1,0,0] neg_hi:[1,0,0]
	v_pk_fma_f16 v7, v3, v142, v143 op_sel:[0,1,1] op_sel_hi:[1,1,1] neg_lo:[1,0,0] neg_hi:[1,0,0]
	v_pk_fma_f16 v8, v4, v142, v143 op_sel:[0,1,1] op_sel_hi:[1,1,1] neg_lo:[1,0,0] neg_hi:[1,0,0]
	v_pk_fma_f16 v9, v5, v142, v143 op_sel:[0,1,1] op_sel_hi:[1,1,1] neg_lo:[1,0,0] neg_hi:[1,0,0]
	v_mfma_f32_16x16x32_f16 v[22:25], v[10:13], v[2:5], 0
	ds_read2_b64 v[52:55], v32 offset0:17 offset1:219
	v_pk_fma_f16 v2, v92, v6, v2
	v_pk_fma_f16 v3, v93, v7, v3
	v_pk_fma_f16 v4, v94, v8, v4
	v_pk_fma_f16 v5, v95, v9, v5
	v_cndmask_b32_e64 v28, v28, v20, s[64:65]
	s_waitcnt lgkmcnt(7)
	v_pk_fma_f16 v6, v2, v144, v145 op_sel:[0,1,1] op_sel_hi:[1,1,1] neg_lo:[1,0,0] neg_hi:[1,0,0]
	v_pk_fma_f16 v7, v3, v144, v145 op_sel:[0,1,1] op_sel_hi:[1,1,1] neg_lo:[1,0,0] neg_hi:[1,0,0]
	v_pk_fma_f16 v8, v4, v144, v145 op_sel:[0,1,1] op_sel_hi:[1,1,1] neg_lo:[1,0,0] neg_hi:[1,0,0]
	v_pk_fma_f16 v9, v5, v144, v145 op_sel:[0,1,1] op_sel_hi:[1,1,1] neg_lo:[1,0,0] neg_hi:[1,0,0]
	v_mfma_f32_16x16x32_f16 v[18:21], v[10:13], v[2:5], 0
	ds_read2_b64 v[56:59], v32 offset0:18 offset1:220
	ds_read_b128 v[124:127], v33 offset:144
	v_pk_fma_f16 v2, v96, v6, v2
	v_pk_fma_f16 v3, v97, v7, v3
	v_pk_fma_f16 v4, v98, v8, v4
	v_pk_fma_f16 v5, v99, v9, v5
	v_cndmask_b32_e64 v29, v29, v25, s[64:65]
	v_pk_fma_f16 v6, v2, v146, v147 op_sel:[0,1,1] op_sel_hi:[1,1,1] neg_lo:[1,0,0] neg_hi:[1,0,0]
	v_pk_fma_f16 v7, v3, v146, v147 op_sel:[0,1,1] op_sel_hi:[1,1,1] neg_lo:[1,0,0] neg_hi:[1,0,0]
	v_pk_fma_f16 v8, v4, v146, v147 op_sel:[0,1,1] op_sel_hi:[1,1,1] neg_lo:[1,0,0] neg_hi:[1,0,0]
	v_pk_fma_f16 v9, v5, v146, v147 op_sel:[0,1,1] op_sel_hi:[1,1,1] neg_lo:[1,0,0] neg_hi:[1,0,0]
	v_mfma_f32_16x16x32_f16 v[22:25], v[10:13], v[2:5], 0
	ds_read2_b64 v[60:63], v32 offset0:19 offset1:221
	v_pk_fma_f16 v2, v100, v6, v2
	v_pk_fma_f16 v3, v101, v7, v3
	v_pk_fma_f16 v4, v102, v8, v4
	v_pk_fma_f16 v5, v103, v9, v5
	v_cndmask_b32_e64 v26, v26, v18, s[66:67]
	s_waitcnt lgkmcnt(7)
	v_pk_fma_f16 v6, v2, v148, v149 op_sel:[0,1,1] op_sel_hi:[1,1,1] neg_lo:[1,0,0] neg_hi:[1,0,0]
	v_pk_fma_f16 v7, v3, v148, v149 op_sel:[0,1,1] op_sel_hi:[1,1,1] neg_lo:[1,0,0] neg_hi:[1,0,0]
	v_pk_fma_f16 v8, v4, v148, v149 op_sel:[0,1,1] op_sel_hi:[1,1,1] neg_lo:[1,0,0] neg_hi:[1,0,0]
	v_pk_fma_f16 v9, v5, v148, v149 op_sel:[0,1,1] op_sel_hi:[1,1,1] neg_lo:[1,0,0] neg_hi:[1,0,0]
	v_mfma_f32_16x16x32_f16 v[18:21], v[10:13], v[2:5], 0
	ds_read2_b64 v[64:67], v32 offset0:20 offset1:222
	ds_read_b128 v[128:131], v33 offset:160
	v_pk_fma_f16 v2, v104, v6, v2
	v_pk_fma_f16 v3, v105, v7, v3
	v_pk_fma_f16 v4, v106, v8, v4
	v_pk_fma_f16 v5, v107, v9, v5
	v_cndmask_b32_e64 v27, v27, v23, s[66:67]
	s_cmp_eq_u32 s72, 1
	s_cbranch_scc0 .Lc1_ns0
	s_waitcnt lgkmcnt(6)
	v_readfirstlane_b32 s4, v45
	s_cmp_eq_u32 s4, 4
	s_cbranch_scc0 .Lc1_dslow0

.Lc1_ns0:
	v_pk_fma_f16 v6, v2, v150, v151 op_sel:[0,1,1] op_sel_hi:[1,1,1] neg_lo:[1,0,0] neg_hi:[1,0,0]
	v_pk_fma_f16 v7, v3, v150, v151 op_sel:[0,1,1] op_sel_hi:[1,1,1] neg_lo:[1,0,0] neg_hi:[1,0,0]
	v_pk_fma_f16 v8, v4, v150, v151 op_sel:[0,1,1] op_sel_hi:[1,1,1] neg_lo:[1,0,0] neg_hi:[1,0,0]
	v_pk_fma_f16 v9, v5, v150, v151 op_sel:[0,1,1] op_sel_hi:[1,1,1] neg_lo:[1,0,0] neg_hi:[1,0,0]
	v_mfma_f32_16x16x32_f16 v[22:25], v[10:13], v[2:5], 0
	ds_read2_b64 v[68:71], v32 offset0:21 offset1:223
	v_pk_fma_f16 v2, v108, v6, v2
	v_pk_fma_f16 v3, v109, v7, v3
	v_pk_fma_f16 v4, v110, v8, v4
	v_pk_fma_f16 v5, v111, v9, v5
	v_cndmask_b32_e64 v28, v28, v20, s[66:67]

.Lc1_back1:
	v_pk_fma_f16 v6, v2, v138, v139 op_sel:[0,1,1] op_sel_hi:[1,1,1] neg_lo:[1,0,0] neg_hi:[1,0,0]
	v_pk_fma_f16 v7, v3, v138, v139 op_sel:[0,1,1] op_sel_hi:[1,1,1] neg_lo:[1,0,0] neg_hi:[1,0,0]
	v_pk_fma_f16 v8, v4, v138, v139 op_sel:[0,1,1] op_sel_hi:[1,1,1] neg_lo:[1,0,0] neg_hi:[1,0,0]
	v_pk_fma_f16 v9, v5, v138, v139 op_sel:[0,1,1] op_sel_hi:[1,1,1] neg_lo:[1,0,0] neg_hi:[1,0,0]
	v_mfma_f32_16x16x32_f16 v[22:25], v[14:17], v[2:5], 0
	ds_read2_b64 v[108:111], v32 offset0:31 offset1:233
	v_pk_fma_f16 v2, v84, v6, v2
	v_pk_fma_f16 v3, v85, v7, v3
	v_pk_fma_f16 v4, v86, v8, v4
	v_pk_fma_f16 v5, v87, v9, v5
	v_cndmask_b32_e64 v26, v26, v18, s[64:65]
	s_waitcnt lgkmcnt(6)
	v_pk_fma_f16 v6, v2, v140, v141 op_sel:[0,1,1] op_sel_hi:[1,1,1] neg_lo:[1,0,0] neg_hi:[1,0,0]
	v_pk_fma_f16 v7, v3, v140, v141 op_sel:[0,1,1] op_sel_hi:[1,1,1] neg_lo:[1,0,0] neg_hi:[1,0,0]
	v_pk_fma_f16 v8, v4, v140, v141 op_sel:[0,1,1] op_sel_hi:[1,1,1] neg_lo:[1,0,0] neg_hi:[1,0,0]
	v_pk_fma_f16 v9, v5, v140, v141 op_sel:[0,1,1] op_sel_hi:[1,1,1] neg_lo:[1,0,0] neg_hi:[1,0,0]
	v_mfma_f32_16x16x32_f16 v[18:21], v[14:17], v[2:5], 0
	ds_read2_b64 v[48:51], v32 offset0:32 offset1:234
	ds_read_b128 v[120:123], v33 offset:256
	ds_read2_b64 v[10:13], v34 offset0:32 offset1:234
	v_pk_fma_f16 v2, v88, v6, v2
	v_pk_fma_f16 v3, v89, v7, v3
	v_pk_fma_f16 v4, v90, v8, v4
	v_pk_fma_f16 v5, v91, v9, v5
	v_cndmask_b32_e64 v27, v27, v23, s[64:65]
	s_mov_b32 s72, 0
	s_cmp_eq_u32 s36, 2
	s_cbranch_scc0 .Lc1_nd1
	s_mov_b32 s72, 1
	ds_read_b32 v45, v36 offset:128
	ds_read_b128 v[112:115], v43 offset:2048
	ds_read_b128 v[116:119], v43 offset:3072
.Lc1_nd1:
	v_pk_fma_f16 v6, v2, v142, v143 op_sel:[0,1,1] op_sel_hi:[1,1,1] neg_lo:[1,0,0] neg_hi:[1,0,0]
	v_pk_fma_f16 v7, v3, v142, v143 op_sel:[0,1,1] op_sel_hi:[1,1,1] neg_lo:[1,0,0] neg_hi:[1,0,0]
	v_pk_fma_f16 v8, v4, v142, v143 op_sel:[0,1,1] op_sel_hi:[1,1,1] neg_lo:[1,0,0] neg_hi:[1,0,0]
	v_pk_fma_f16 v9, v5, v142, v143 op_sel:[0,1,1] op_sel_hi:[1,1,1] neg_lo:[1,0,0] neg_hi:[1,0,0]
	v_mfma_f32_16x16x32_f16 v[22:25], v[14:17], v[2:5], 0
	ds_read2_b64 v[52:55], v32 offset0:33 offset1:235
	v_pk_fma_f16 v2, v92, v6, v2
	v_pk_fma_f16 v3, v93, v7, v3
	v_pk_fma_f16 v4, v94, v8, v4
	v_pk_fma_f16 v5, v95, v9, v5
	v_cndmask_b32_e64 v28, v28, v20, s[64:65]
	s_waitcnt lgkmcnt(7)
	v_pk_fma_f16 v6, v2, v144, v145 op_sel:[0,1,1] op_sel_hi:[1,1,1] neg_lo:[1,0,0] neg_hi:[1,0,0]
	v_pk_fma_f16 v7, v3, v144, v145 op_sel:[0,1,1] op_sel_hi:[1,1,1] neg_lo:[1,0,0] neg_hi:[1,0,0]
	v_pk_fma_f16 v8, v4, v144, v145 op_sel:[0,1,1] op_sel_hi:[1,1,1] neg_lo:[1,0,0] neg_hi:[1,0,0]
	v_pk_fma_f16 v9, v5, v144, v145 op_sel:[0,1,1] op_sel_hi:[1,1,1] neg_lo:[1,0,0] neg_hi:[1,0,0]
	v_mfma_f32_16x16x32_f16 v[18:21], v[14:17], v[2:5], 0
	ds_read2_b64 v[56:59], v32 offset0:34 offset1:236
	ds_read_b128 v[124:127], v33 offset:272
	v_pk_fma_f16 v2, v96, v6, v2
	v_pk_fma_f16 v3, v97, v7, v3
	v_pk_fma_f16 v4, v98, v8, v4
	v_pk_fma_f16 v5, v99, v9, v5
	v_cndmask_b32_e64 v29, v29, v25, s[64:65]
	v_pk_fma_f16 v6, v2, v146, v147 op_sel:[0,1,1] op_sel_hi:[1,1,1] neg_lo:[1,0,0] neg_hi:[1,0,0]
	v_pk_fma_f16 v7, v3, v146, v147 op_sel:[0,1,1] op_sel_hi:[1,1,1] neg_lo:[1,0,0] neg_hi:[1,0,0]
	v_pk_fma_f16 v8, v4, v146, v147 op_sel:[0,1,1] op_sel_hi:[1,1,1] neg_lo:[1,0,0] neg_hi:[1,0,0]
	v_pk_fma_f16 v9, v5, v146, v147 op_sel:[0,1,1] op_sel_hi:[1,1,1] neg_lo:[1,0,0] neg_hi:[1,0,0]
	v_mfma_f32_16x16x32_f16 v[22:25], v[14:17], v[2:5], 0
	ds_read2_b64 v[60:63], v32 offset0:35 offset1:237
	v_pk_fma_f16 v2, v100, v6, v2
	v_pk_fma_f16 v3, v101, v7, v3
	v_pk_fma_f16 v4, v102, v8, v4
	v_pk_fma_f16 v5, v103, v9, v5
	v_cndmask_b32_e64 v26, v26, v18, s[66:67]
	s_waitcnt lgkmcnt(7)
	v_pk_fma_f16 v6, v2, v148, v149 op_sel:[0,1,1] op_sel_hi:[1,1,1] neg_lo:[1,0,0] neg_hi:[1,0,0]
	v_pk_fma_f16 v7, v3, v148, v149 op_sel:[0,1,1] op_sel_hi:[1,1,1] neg_lo:[1,0,0] neg_hi:[1,0,0]
	v_pk_fma_f16 v8, v4, v148, v149 op_sel:[0,1,1] op_sel_hi:[1,1,1] neg_lo:[1,0,0] neg_hi:[1,0,0]
	v_pk_fma_f16 v9, v5, v148, v149 op_sel:[0,1,1] op_sel_hi:[1,1,1] neg_lo:[1,0,0] neg_hi:[1,0,0]
	v_mfma_f32_16x16x32_f16 v[18:21], v[14:17], v[2:5], 0
	ds_read2_b64 v[64:67], v32 offset0:36 offset1:238
	ds_read_b128 v[128:131], v33 offset:288
	v_pk_fma_f16 v2, v104, v6, v2
	v_pk_fma_f16 v3, v105, v7, v3
	v_pk_fma_f16 v4, v106, v8, v4
	v_pk_fma_f16 v5, v107, v9, v5
	v_cndmask_b32_e64 v27, v27, v23, s[66:67]
	s_cmp_eq_u32 s72, 1
	s_cbranch_scc0 .Lc1_ns1
	s_waitcnt lgkmcnt(6)
	v_readfirstlane_b32 s4, v45
	s_cmp_eq_u32 s4, 4
	s_cbranch_scc0 .Lc1_dslow1

.Lc1_ns1:
	v_pk_fma_f16 v6, v2, v150, v151 op_sel:[0,1,1] op_sel_hi:[1,1,1] neg_lo:[1,0,0] neg_hi:[1,0,0]
	v_pk_fma_f16 v7, v3, v150, v151 op_sel:[0,1,1] op_sel_hi:[1,1,1] neg_lo:[1,0,0] neg_hi:[1,0,0]
	v_pk_fma_f16 v8, v4, v150, v151 op_sel:[0,1,1] op_sel_hi:[1,1,1] neg_lo:[1,0,0] neg_hi:[1,0,0]
	v_pk_fma_f16 v9, v5, v150, v151 op_sel:[0,1,1] op_sel_hi:[1,1,1] neg_lo:[1,0,0] neg_hi:[1,0,0]
	v_mfma_f32_16x16x32_f16 v[22:25], v[14:17], v[2:5], 0
	ds_read2_b64 v[68:71], v32 offset0:37 offset1:239
	v_pk_fma_f16 v2, v108, v6, v2
	v_pk_fma_f16 v3, v109, v7, v3
	v_pk_fma_f16 v4, v110, v8, v4
	v_pk_fma_f16 v5, v111, v9, v5
	v_cndmask_b32_e64 v28, v28, v20, s[66:67]
